# speedup vs baseline: 1.0385x; 1.0162x over previous
.LBB1_89:
	s_or_b64 exec, exec, s[18:19]
	s_barrier
	s_add_u32 s4, s0, s40
	s_addc_u32 s5, s1, s41
	v_and_b32_e32 v101, 48, v179
	v_lshlrev_b32_e32 v101, 4, v101
	v_and_b32_e32 v126, 7, v179
	v_lshl_or_b32 v101, v126, 10, v101
	v_bfe_u32 v126, v179, 3, 1
	v_lshl_or_b32 v101, v126, 17, v101
	v_add_u32_e32 v101, s90, v101
	s_add_u32 s0, s0, s42
	s_addc_u32 s1, s1, s43
	global_load_dwordx4 v[150:153], v101, s[4:5]
	global_load_dwordx4 v[138:141], v108, s[0:1]
	global_load_dwordx4 v[142:145], v108, s[0:1] offset:1024
	global_load_dwordx4 v[146:149], v108, s[0:1] offset:2048
	global_load_dwordx4 v[126:129], v108, s[0:1] offset:3072
	v_add_u32_e32 v100, s95, v108
	v_add_u32_e32 v98, s10, v108
	ds_read_b128 v[224:227], v100
	ds_read_b128 v[228:231], v98
	ds_read_b128 v[232:235], v100 offset:1024
	ds_read_b128 v[236:239], v98 offset:1024
	s_andn2_b64 vcc, exec, s[38:39]
	s_waitcnt vmcnt(4)
	v_mov_b32_dpp v196, v150 row_shl:1 row_mask:0xf bank_mask:0xf bound_ctrl:1
	v_mov_b32_dpp v197, v151 row_shl:1 row_mask:0xf bank_mask:0xf bound_ctrl:1
	v_mov_b32_dpp v198, v152 row_shl:1 row_mask:0xf bank_mask:0xf bound_ctrl:1
	v_mov_b32_dpp v199, v153 row_shl:1 row_mask:0xf bank_mask:0xf bound_ctrl:1
	s_waitcnt lgkmcnt(2)
	v_mfma_f32_16x16x32_f16 v[204:207], v[224:227], v[150:153], 0
	v_mfma_f32_16x16x32_f16 v[212:215], v[228:231], v[150:153], 0
	ds_read_b128 v[224:227], v100 offset:2048
	ds_read_b128 v[228:231], v98 offset:2048
	v_mov_b32_dpp v154, v150 row_shl:2 row_mask:0xf bank_mask:0xf bound_ctrl:1
	v_mov_b32_dpp v155, v151 row_shl:2 row_mask:0xf bank_mask:0xf bound_ctrl:1
	v_mov_b32_dpp v156, v152 row_shl:2 row_mask:0xf bank_mask:0xf bound_ctrl:1
	v_mov_b32_dpp v157, v153 row_shl:2 row_mask:0xf bank_mask:0xf bound_ctrl:1
	s_waitcnt lgkmcnt(2)
	v_mfma_f32_16x16x32_f16 v[208:211], v[232:235], v[196:199], 0
	v_mfma_f32_16x16x32_f16 v[220:223], v[236:239], v[196:199], 0
	ds_read_b128 v[232:235], v100 offset:3072
	ds_read_b128 v[236:239], v98 offset:3072
	v_mov_b32_dpp v196, v150 row_shl:3 row_mask:0xf bank_mask:0xf bound_ctrl:1
	v_mov_b32_dpp v197, v151 row_shl:3 row_mask:0xf bank_mask:0xf bound_ctrl:1
	v_mov_b32_dpp v198, v152 row_shl:3 row_mask:0xf bank_mask:0xf bound_ctrl:1
	v_mov_b32_dpp v199, v153 row_shl:3 row_mask:0xf bank_mask:0xf bound_ctrl:1
	s_waitcnt lgkmcnt(2)
	v_mfma_f32_16x16x32_f16 v[204:207], v[224:227], v[154:157], v[204:207]
	v_mfma_f32_16x16x32_f16 v[212:215], v[228:231], v[154:157], v[212:215]
	ds_read_b128 v[224:227], v100 offset:4096
	ds_read_b128 v[228:231], v98 offset:4096
	v_mov_b32_dpp v154, v150 row_shl:4 row_mask:0xf bank_mask:0xf bound_ctrl:1
	v_mov_b32_dpp v155, v151 row_shl:4 row_mask:0xf bank_mask:0xf bound_ctrl:1
	v_mov_b32_dpp v156, v152 row_shl:4 row_mask:0xf bank_mask:0xf bound_ctrl:1
	v_mov_b32_dpp v157, v153 row_shl:4 row_mask:0xf bank_mask:0xf bound_ctrl:1
	s_waitcnt lgkmcnt(2)
	v_mfma_f32_16x16x32_f16 v[208:211], v[232:235], v[196:199], v[208:211]
	v_mfma_f32_16x16x32_f16 v[220:223], v[236:239], v[196:199], v[220:223]
	ds_read_b128 v[232:235], v100 offset:5120
	ds_read_b128 v[236:239], v98 offset:5120
	v_mov_b32_dpp v196, v150 row_shl:5 row_mask:0xf bank_mask:0xf bound_ctrl:1
	v_mov_b32_dpp v197, v151 row_shl:5 row_mask:0xf bank_mask:0xf bound_ctrl:1
	v_mov_b32_dpp v198, v152 row_shl:5 row_mask:0xf bank_mask:0xf bound_ctrl:1
	v_mov_b32_dpp v199, v153 row_shl:5 row_mask:0xf bank_mask:0xf bound_ctrl:1
	s_waitcnt lgkmcnt(2)
	v_mfma_f32_16x16x32_f16 v[204:207], v[224:227], v[154:157], v[204:207]
	v_mfma_f32_16x16x32_f16 v[212:215], v[228:231], v[154:157], v[212:215]
	ds_read_b128 v[224:227], v100 offset:6144
	ds_read_b128 v[228:231], v98 offset:6144
	v_mov_b32_dpp v154, v150 row_shl:6 row_mask:0xf bank_mask:0xf bound_ctrl:1
	v_mov_b32_dpp v155, v151 row_shl:6 row_mask:0xf bank_mask:0xf bound_ctrl:1
	v_mov_b32_dpp v156, v152 row_shl:6 row_mask:0xf bank_mask:0xf bound_ctrl:1
	v_mov_b32_dpp v157, v153 row_shl:6 row_mask:0xf bank_mask:0xf bound_ctrl:1
	s_waitcnt lgkmcnt(2)
	v_mfma_f32_16x16x32_f16 v[208:211], v[232:235], v[196:199], v[208:211]
	v_mfma_f32_16x16x32_f16 v[220:223], v[236:239], v[196:199], v[220:223]
	ds_read_b128 v[232:235], v100 offset:7168
	s_cbranch_vccnz .Lc1_skip_afl7
	ds_read_b128 v[110:113], v98 offset:7168
.Lc1_skip_afl7:
	v_mov_b32_dpp v196, v150 row_shl:7 row_mask:0xf bank_mask:0xf bound_ctrl:1
	v_mov_b32_dpp v197, v151 row_shl:7 row_mask:0xf bank_mask:0xf bound_ctrl:1
	v_mov_b32_dpp v198, v152 row_shl:7 row_mask:0xf bank_mask:0xf bound_ctrl:1
	v_mov_b32_dpp v199, v153 row_shl:7 row_mask:0xf bank_mask:0xf bound_ctrl:1
	s_waitcnt lgkmcnt(1)
	v_mfma_f32_16x16x32_f16 v[162:165], v[224:227], v[154:157], v[204:207]
	v_mfma_f32_16x16x32_f16 v[166:169], v[228:231], v[154:157], v[212:215]
	s_waitcnt lgkmcnt(0)
	v_mfma_f32_16x16x32_f16 v[158:161], v[232:235], v[196:199], v[208:211]
	v_mfma_f32_16x16x32_f16 v[130:133], v[110:113], v[196:199], v[220:223]
	s_waitcnt vmcnt(3)
	v_mfma_f32_16x16x32_f16 v[114:117], v[114:117], v[138:141], 0
	v_and_b32_e32 v98, 15, v179
	v_cmp_eq_u32_e32 vcc, 0, v98
	s_waitcnt vmcnt(2)
	v_mfma_f32_16x16x32_f16 v[114:117], v[118:121], v[142:145], v[114:117]
	s_waitcnt vmcnt(1)
	v_mfma_f32_16x16x32_f16 v[114:117], v[122:125], v[146:149], v[114:117]
	s_waitcnt vmcnt(0)
	v_mfma_f32_16x16x32_f16 v[104:107], v[104:107], v[126:129], v[114:117]
	s_nop 7
	v_mov_b32_dpp v170, v162 row_shl:8 row_mask:0xf bank_mask:0xf bound_ctrl:1
	v_mov_b32_dpp v171, v163 row_shl:8 row_mask:0xf bank_mask:0xf bound_ctrl:1
	v_mov_b32_dpp v172, v164 row_shl:8 row_mask:0xf bank_mask:0xf bound_ctrl:1
	v_mov_b32_dpp v173, v165 row_shl:8 row_mask:0xf bank_mask:0xf bound_ctrl:1
	v_mov_b32_dpp v110, v158 row_shl:8 row_mask:0xf bank_mask:0xf bound_ctrl:1
	v_mov_b32_dpp v111, v159 row_shl:8 row_mask:0xf bank_mask:0xf bound_ctrl:1
	v_mov_b32_dpp v112, v160 row_shl:8 row_mask:0xf bank_mask:0xf bound_ctrl:1
	v_mov_b32_dpp v113, v161 row_shl:8 row_mask:0xf bank_mask:0xf bound_ctrl:1
	s_and_saveexec_b64 s[0:1], vcc
	s_cbranch_execz .LBB1_93
	v_pk_add_f32 v[100:101], v[172:173], v[168:169]
	v_pk_add_f32 v[114:115], v[170:171], v[166:167]
	s_nop 0
	v_pk_add_f32 v[100:101], v[132:133], v[100:101]
	v_pk_add_f32 v[114:115], v[130:131], v[114:115]
	v_pk_add_f32 v[100:101], v[112:113], v[100:101]
	v_pk_add_f32 v[110:111], v[110:111], v[114:115]
	v_readlane_b32 s4, v240, 17
	v_pk_fma_f32 v[110:111], v[110:111], s[92:93], v[158:159] op_sel_hi:[1,0,1]
	v_pk_fma_f32 v[100:101], v[100:101], s[92:93], v[160:161] op_sel_hi:[1,0,1]
	v_add_u32_e32 v108, s4, v103
	v_pk_add_f32 v[110:111], v[162:163], v[110:111]
	v_pk_add_f32 v[100:101], v[164:165], v[100:101]
	ds_write2_b32 v108, v110, v111 offset1:1
	ds_write2_b32 v108, v100, v101 offset0:2 offset1:3
